# v11 + moba_c next-item decode: galloping probe from the current list index before the binary search
# speedup vs baseline: 1.0017x; 1.0017x over previous
.LBB0_1381:
	s_add_i32 s6, s6, 1
	s_cmp_ge_i32 s6, s8
	s_cselect_b64 s[18:19], -1, 0
	s_and_b64 vcc, exec, s[18:19]
	s_cbranch_vccnz .LBB0_1386
	s_add_i32 s11, s17, 4
	s_min_i32 s11, s11, 0xff
	s_lshl_b32 s21, s11, 2
	s_add_i32 s21, s21, 0x21000
	v_mov_b32_e32 v2, s21
	ds_read_b32 v2, v2
	s_waitcnt lgkmcnt(0)
	v_readfirstlane_b32 s22, v2
	s_cmp_gt_i32 s22, s6
	s_cbranch_scc0 .Lmc_full
	s_add_i32 s11, s11, -1
	s_mov_b32 s10, s17
	s_branch .LBB0_1383
.Lmc_full:
	s_mov_b32 s10, s11
	s_movk_i32 s11, 0xff
